# P9 down-GEMM unit order grouped per XCD (4 row blocks x 8 column tiles per XCD per round)
# speedup vs baseline: 1.0049x; 1.0049x over previous
.LBB0_1408:
	s_or_b64 exec, exec, s[4:5]
	s_add_u32 s4, s84, 0x57800000
	s_addc_u32 s5, s85, 0
	s_add_i32 s6, 0, 0x20100
	v_mov_b32_e32 v11, v0
	s_waitcnt lgkmcnt(0)
	v_mov_b32_e32 v1, s6
	s_barrier
	ds_read_b32 v1, v1
	s_lshr_b32 s100, s96, 3
	s_and_b32 s24, s100, 0x18
	s_and_b32 s101, s96, 7
	s_add_i32 s24, s24, s101
	v_readfirstlane_b32 s10, v11
	s_waitcnt lgkmcnt(0)
	v_readfirstlane_b32 s6, v1
	s_cmp_ge_i32 s24, s6
	s_cbranch_scc1 .LBB0_1426
	v_lshlrev_b32_e32 v1, 4, v11
	v_add_u32_e32 v2, 0x2000, v1
	v_ashrrev_i32_e32 v3, 31, v2
	v_lshrrev_b32_e32 v3, 22, v3
	v_add_u32_e32 v3, v2, v3
	v_ashrrev_i32_e32 v10, 10, v3
	v_mul_i32_i24_e32 v3, 0x400, v10
	v_sub_u32_e32 v2, v2, v3
	v_lshrrev_b32_e32 v3, 4, v2
	v_bitop3_b32 v2, v3, v2, 32 bitop3:0x6c
	v_ashrrev_i32_e32 v3, 31, v2
	v_lshrrev_b32_e32 v3, 26, v3
	v_add_u32_e32 v3, v2, v3
	v_lshlrev_b32_e32 v4, 3, v10
	v_ashrrev_i32_e32 v12, 6, v3
	v_and_b32_e32 v4, -16, v4
	v_add_u32_e32 v4, v12, v4
	v_and_b32_e32 v5, 3, v12
	s_mov_b32 s6, 0x1fffe0
	v_lshrrev_b32_e32 v6, 2, v4
	v_lshlrev_b32_e32 v7, 1, v4
	v_and_b32_e32 v3, 0xc0, v3
	v_and_or_b32 v5, v4, s6, v5
	v_and_b32_e32 v6, 4, v6
	v_and_b32_e32 v7, 24, v7
	v_sub_u32_e32 v2, v2, v3
	v_mov_b32_e32 v3, 1
	v_or3_b32 v5, v5, v6, v7
	v_lshlrev_b32_e32 v6, 5, v10
	v_ashrrev_i16_sdwa v2, v3, sext(v2) dst_sel:DWORD dst_unused:UNUSED_PAD src0_sel:DWORD src1_sel:BYTE_0
	v_and_b32_e32 v6, 32, v6
	v_bfe_i32 v13, v2, 0, 16
	v_add_lshl_u32 v2, v6, v13, 1
	v_lshl_add_u32 v162, v5, 11, v2
	v_bfe_i32 v5, v11, 27, 1
	v_lshrrev_b32_e32 v5, 22, v5
	v_add_u32_e32 v5, v1, v5
	v_and_b32_e32 v5, 0xfffffc00, v5
	v_sub_u32_e32 v1, v1, v5
	v_lshrrev_b32_e32 v5, 4, v1
	v_ashrrev_i32_e32 v6, 31, v11
	v_bitop3_b32 v1, v5, v1, 32 bitop3:0x6c
	v_lshrrev_b32_e32 v6, 26, v6
	v_ashrrev_i32_e32 v5, 31, v1
	v_add_u32_e32 v6, v11, v6
	v_lshrrev_b32_e32 v5, 26, v5
	v_ashrrev_i32_e32 v15, 6, v6
	v_add_u32_e32 v5, v1, v5
	v_lshlrev_b32_e32 v6, 3, v15
	v_ashrrev_i32_e32 v14, 6, v5
	v_and_b32_e32 v6, -16, v6
	s_add_u32 s33, s84, 0x89800000
	v_add_u32_e32 v6, v14, v6
	v_and_b32_e32 v7, 3, v14
	s_addc_u32 s36, s85, 0
	v_and_or_b32 v7, v6, s6, v7
	s_lshl_b32 s6, s24, 2
	v_and_b32_e32 v5, 0xc0, v5
	s_add_i32 s6, s6, 0
	v_sub_u32_e32 v1, v1, v5
	s_add_i32 s6, s6, 0x20120
	v_ashrrev_i16_sdwa v1, v3, sext(v1) dst_sel:DWORD dst_unused:UNUSED_PAD src0_sel:DWORD src1_sel:BYTE_0
	v_mov_b32_e32 v3, s6
	ds_read_b32 v3, v3
	s_ashr_i32 s8, s10, 6
	s_ashr_i32 s25, s24, 31
	s_ashr_i32 s11, s10, 8
	s_lshl_b32 s37, s8, 10
	s_and_b32 s49, s100, 7
	s_lshl_b64 s[6:7], s[24:25], 19
	s_waitcnt lgkmcnt(0)
	v_readfirstlane_b32 s28, v3
	s_add_u32 s26, s0, s6
	s_addc_u32 s27, s1, s7
	s_ashr_i32 s29, s28, 31
	v_lshrrev_b32_e32 v8, 2, v6
	v_lshlrev_b32_e32 v9, 1, v6
	s_lshl_b32 s9, s49, 19
	s_lshl_b64 s[6:7], s[28:29], 22
	v_and_b32_e32 v8, 4, v8
	v_and_b32_e32 v9, 24, v9
	s_add_u32 s6, s33, s6
	v_or3_b32 v7, v7, v8, v9
	v_lshlrev_b32_e32 v8, 5, v15
	s_addc_u32 s7, s36, s7
	v_and_b32_e32 v8, 32, v8
	v_bfe_i32 v16, v1, 0, 16
	s_add_u32 s30, s6, s9
	v_add_lshl_u32 v1, v8, v16, 1
	s_addc_u32 s31, s7, 0
	s_add_i32 s38, s37, 0
	v_lshl_add_u32 v164, v7, 11, v1
	s_add_i32 m0, s38, 0x10000
	v_lshl_add_u32 v166, v6, 11, v1
	global_load_lds_dwordx4 v164, s[30:31]
	s_add_i32 m0, s38, 0x12000
	s_add_u32 s6, s30, 0x40000
	global_load_lds_dwordx4 v162, s[30:31]
	s_addc_u32 s7, s31, 0
	s_add_i32 m0, s38, 0x14000
	s_add_i32 s39, s38, 0x2000
	global_load_lds_dwordx4 v164, s[6:7]
	s_add_i32 m0, s38, 0x16000
	v_lshl_add_u32 v168, v4, 11, v2
	global_load_lds_dwordx4 v162, s[6:7]
	s_mov_b32 m0, s38
	s_add_i32 s40, s38, 0x4000
	global_load_lds_dwordx4 v166, s[26:27]
	s_mov_b32 m0, s39
	v_add_u32_e32 v170, 0x40000, v166
	global_load_lds_dwordx4 v168, s[26:27]
	s_mov_b32 m0, s40
	s_add_i32 s41, s38, 0x6000
	v_add_u32_e32 v172, 0x40000, v168
	global_load_lds_dwordx4 v170, s[26:27]
	s_mov_b32 m0, s41
	v_mov_b32_e32 v165, 0
	global_load_lds_dwordx4 v172, s[26:27]
	v_mov_b32_e32 v163, v165
	v_mov_b32_e32 v167, v165
	v_mov_b32_e32 v169, v165
	s_cmp_eq_u32 s11, 1
	s_mov_b32 s42, 0x40000
	v_lshl_add_u64 v[8:9], s[30:31], 0, v[164:165]
	v_lshl_add_u64 v[6:7], s[30:31], 0, v[162:163]
	v_lshl_add_u64 v[2:3], s[26:27], 0, v[166:167]
	s_cselect_b64 s[6:7], -1, 0
	s_cmp_lg_u32 s11, 1
	v_lshl_add_u64 v[4:5], s[26:27], 0, v[168:169]
	s_cbranch_scc1 .LBB0_1411
	s_barrier

.LBB0_1414:
	ds_read_b32 v2, v190
	s_add_i32 s48, s25, 1
	v_readlane_b32 s22, v252, 41
	s_mul_i32 s29, s48, s22
	s_add_i32 s29, s29, s96
	s_lshr_b32 s100, s29, 3
	s_and_b32 s34, s100, 0x18
	s_and_b32 s101, s29, 7
	s_add_i32 s34, s34, s101
	s_lshr_b32 s101, s29, 8
	s_lshl_b32 s101, s101, 5
	s_add_i32 s34, s34, s101
	s_waitcnt lgkmcnt(0)
	v_readfirstlane_b32 s35, v2
	s_cmp_lt_i32 s34, s35
	s_cselect_b64 s[22:23], -1, 0
	s_cmp_ge_i32 s34, s35
	s_cbranch_scc1 .LBB0_1416
	s_lshl_b32 s16, s34, 2
	s_add_i32 s16, s16, 0
	s_add_i32 s16, s16, 0x20120
	v_mov_b32_e32 v2, s16
	ds_read_b32 v2, v2
	s_ashr_i32 s35, s34, 31
	s_and_b32 s47, s100, 7
	s_lshl_b64 s[16:17], s[34:35], 19
	s_add_u32 s18, s0, s16
	s_waitcnt lgkmcnt(0)
	v_readfirstlane_b32 s16, v2
	s_addc_u32 s19, s1, s17
	s_ashr_i32 s17, s16, 31
	s_lshl_b32 s29, s47, 19
	s_lshl_b64 s[20:21], s[16:17], 22
	s_add_u32 s17, s33, s20
	s_addc_u32 s21, s36, s21
	s_add_u32 s20, s17, s29
	s_addc_u32 s21, s21, 0
	s_mov_b32 s17, s34
